# speedup vs baseline: 1.0112x; 1.0112x over previous
.Lret0:
	s_setprio 1
	s_waitcnt vmcnt(19)
	v_cvt_pk_f16_f32 v79, v8, v9
	v_cvt_pk_f16_f32 v78, v6, v7
	ds_write_b64 v141, v[78:79] offset:19456
	s_waitcnt vmcnt(18)
	v_cvt_pk_f16_f32 v79, v12, v13
	v_cvt_pk_f16_f32 v78, v10, v11
	ds_write_b64 v143, v[78:79] offset:19456
	s_waitcnt vmcnt(17)
	v_cvt_pk_f16_f32 v79, v20, v21
	v_cvt_pk_f16_f32 v78, v18, v19
	ds_write_b64 v144, v[78:79] offset:19456
	s_waitcnt vmcnt(16)
	v_cvt_pk_f16_f32 v79, v24, v25
	v_cvt_pk_f16_f32 v78, v22, v23
	ds_write_b64 v145, v[78:79] offset:19456
	s_waitcnt vmcnt(15)
	v_cvt_pk_f16_f32 v79, v28, v29
	v_cvt_pk_f16_f32 v78, v26, v27
	ds_write_b64 v146, v[78:79] offset:19456
	s_waitcnt vmcnt(14)
	v_cvt_pk_f16_f32 v79, v32, v33
	v_cvt_pk_f16_f32 v78, v30, v31
	ds_write_b64 v147, v[78:79] offset:19456
	s_waitcnt vmcnt(13)
	v_cvt_pk_f16_f32 v79, v40, v41
	v_cvt_pk_f16_f32 v78, v38, v39
	ds_write_b64 v141, v[78:79] offset:22568
	s_waitcnt vmcnt(12)
	v_cvt_pk_f16_f32 v79, v44, v45
	v_cvt_pk_f16_f32 v78, v42, v43
	ds_write_b64 v148, v[78:79] offset:19456
	s_waitcnt vmcnt(11)
	v_cvt_pk_f16_f32 v79, v52, v53
	v_cvt_pk_f16_f32 v78, v50, v51
	ds_write_b64 v149, v[78:79] offset:19456
	s_waitcnt vmcnt(10)
	v_cvt_pk_f16_f32 v79, v188, v189
	v_cvt_pk_f16_f32 v78, v186, v187
	s_and_saveexec_b64 s[12:13], s[8:9]
	ds_write_b64 v150, v[78:79] offset:19456
	s_or_b64 exec, exec, s[12:13]
	s_mov_b32 s26, 0x7080
	s_mov_b32 s27, 0x8080
	s_mov_b32 s28, 0x9080
	buffer_load_dwordx4 v[6:9], v192, s[16:19], s26 offen nt
	buffer_load_dwordx4 v[10:13], v192, s[16:19], s26 offen offset:1024 nt
	buffer_load_dwordx4 v[18:21], v192, s[16:19], s26 offen offset:2048 nt
	buffer_load_dwordx4 v[22:25], v192, s[16:19], s26 offen offset:3072 nt
	buffer_load_dwordx4 v[26:29], v192, s[16:19], s27 offen nt
	buffer_load_dwordx4 v[30:33], v192, s[16:19], s27 offen offset:1024 nt
	buffer_load_dwordx4 v[38:41], v192, s[16:19], s27 offen offset:2048 nt
	buffer_load_dwordx4 v[42:45], v192, s[16:19], s27 offen offset:3072 nt
	buffer_load_dwordx4 v[50:53], v192, s[16:19], s28 offen nt
	buffer_load_dwordx4 v[186:189], v193, s[16:19], s26 offen offset:1024 nt
	s_mov_b32 s3, 1
	s_branch .LBB0_7
.Lret1:
	s_setprio 2
	s_waitcnt vmcnt(19)
	v_cvt_pk_f16_f32 v79, v4, v5
	v_cvt_pk_f16_f32 v78, v2, v3
	ds_write_b64 v141, v[78:79] offset:19456
	s_waitcnt vmcnt(18)
	v_cvt_pk_f16_f32 v79, v16, v17
	v_cvt_pk_f16_f32 v78, v14, v15
	ds_write_b64 v143, v[78:79] offset:19456
	s_waitcnt vmcnt(17)
	v_cvt_pk_f16_f32 v79, v36, v37
	v_cvt_pk_f16_f32 v78, v34, v35
	ds_write_b64 v144, v[78:79] offset:19456
	s_waitcnt vmcnt(16)
	v_cvt_pk_f16_f32 v79, v48, v49
	v_cvt_pk_f16_f32 v78, v46, v47
	ds_write_b64 v145, v[78:79] offset:19456
	s_waitcnt vmcnt(15)
	v_cvt_pk_f16_f32 v79, v56, v57
	v_cvt_pk_f16_f32 v78, v54, v55
	ds_write_b64 v146, v[78:79] offset:19456
	s_waitcnt vmcnt(14)
	v_cvt_pk_f16_f32 v79, v60, v61
	v_cvt_pk_f16_f32 v78, v58, v59
	ds_write_b64 v147, v[78:79] offset:19456
	s_waitcnt vmcnt(13)
	v_cvt_pk_f16_f32 v79, v64, v65
	v_cvt_pk_f16_f32 v78, v62, v63
	ds_write_b64 v141, v[78:79] offset:22568
	s_waitcnt vmcnt(12)
	v_cvt_pk_f16_f32 v79, v68, v69
	v_cvt_pk_f16_f32 v78, v66, v67
	ds_write_b64 v148, v[78:79] offset:19456
	s_waitcnt vmcnt(11)
	v_cvt_pk_f16_f32 v79, v72, v73
	v_cvt_pk_f16_f32 v78, v70, v71
	ds_write_b64 v149, v[78:79] offset:19456
	s_waitcnt vmcnt(10)
	v_cvt_pk_f16_f32 v79, v76, v77
	v_cvt_pk_f16_f32 v78, v74, v75
	s_and_saveexec_b64 s[12:13], s[8:9]
	ds_write_b64 v150, v[78:79] offset:19456
	s_or_b64 exec, exec, s[12:13]
	s_mov_b32 s3, 2
	s_branch .LBB0_7
.Lret2:
	s_setprio 3
	v_lshrrev_b32_e32 v151, 4, v120
	v_lshl_add_u32 v152, v123, 4, v131
	v_lshlrev_b32_e32 v153, 4, v123
	v_lshlrev_b32_e32 v154, 1, v121
	v_lshrrev_b32_e32 v155, 4, v122
	v_lshl_add_u32 v152, v151, 2, v152
	v_or_b32_e32 v155, v154, v155
	v_sub_u32_e32 v174, 11, v154
	v_lshl_or_b32 v156, v155, 8, v153
	v_cvt_f32_i32_e32 v174, v174
	v_cmp_lt_u32_e32 vcc, 31, v0
	v_add_u32_e32 v157, 0x4c00, v156
	v_mul_f32_e32 v175, 0xbf38aa3b, v174
	v_add_u32_e32 v158, 0xe400, v156
	v_mul_f32_e32 v175, v175, v174
	v_exp_f32_e32 v175, v175
	s_nop 0
	v_cndmask_b32_e32 v174, 1.0, v175, vcc
	s_waitcnt vmcnt(9)
	v_cvt_pk_f16_f32 v79, v8, v9
	v_cvt_pk_f16_f32 v78, v6, v7
	ds_write_b64 v141, v[78:79] offset:19456
	s_waitcnt vmcnt(8)
	v_cvt_pk_f16_f32 v79, v12, v13
	v_cvt_pk_f16_f32 v78, v10, v11
	ds_write_b64 v143, v[78:79] offset:19456
	s_waitcnt vmcnt(7)
	v_cvt_pk_f16_f32 v79, v20, v21
	v_cvt_pk_f16_f32 v78, v18, v19
	ds_write_b64 v144, v[78:79] offset:19456
	s_waitcnt vmcnt(6)
	v_cvt_pk_f16_f32 v79, v24, v25
	v_cvt_pk_f16_f32 v78, v22, v23
	ds_write_b64 v145, v[78:79] offset:19456
	s_waitcnt vmcnt(5)
	v_cvt_pk_f16_f32 v79, v28, v29
	v_cvt_pk_f16_f32 v78, v26, v27
	ds_write_b64 v146, v[78:79] offset:19456
	s_waitcnt vmcnt(4)
	v_cvt_pk_f16_f32 v79, v32, v33
	v_cvt_pk_f16_f32 v78, v30, v31
	ds_write_b64 v147, v[78:79] offset:19456
	s_waitcnt vmcnt(3)
	v_cvt_pk_f16_f32 v79, v40, v41
	v_cvt_pk_f16_f32 v78, v38, v39
	ds_write_b64 v141, v[78:79] offset:22568
	s_waitcnt vmcnt(2)
	v_cvt_pk_f16_f32 v79, v44, v45
	v_cvt_pk_f16_f32 v78, v42, v43
	ds_write_b64 v148, v[78:79] offset:19456
	s_waitcnt vmcnt(1)
	v_cvt_pk_f16_f32 v79, v52, v53
	v_cvt_pk_f16_f32 v78, v50, v51
	ds_write_b64 v149, v[78:79] offset:19456
	s_mov_b32 s3, 3
	v_mov_b32_e32 v86, 0
	v_mov_b32_e32 v78, 0
	v_mov_b32_e32 v79, 0
	v_mov_b32_e32 v80, 0
	v_mov_b32_e32 v81, 0
	v_mov_b32_e32 v82, 0
	v_mov_b32_e32 v83, 0
	v_mov_b32_e32 v84, 0
	v_mov_b32_e32 v85, 0
	ds_read_b128 v[194:197], v142
	ds_read_b128 v[198:201], v136
	ds_read_b128 v[202:205], v136 offset:9728
	ds_read_b128 v[206:209], v142 offset:64
	ds_read_b128 v[210:213], v136 offset:64
	ds_read_b128 v[214:217], v136 offset:9792
	ds_read_b128 v[218:221], v142 offset:128
	ds_read_b128 v[222:225], v136 offset:128
	ds_read_b128 v[226:229], v136 offset:9856
	ds_read_b128 v[230:233], v142 offset:192
	ds_read_b128 v[234:237], v136 offset:192
	ds_read_b128 v[238:241], v136 offset:9920
	s_waitcnt lgkmcnt(9)
	v_mfma_f32_16x16x32_f16 v[78:81], v[194:197], v[198:201], v[78:81]
	v_dot2c_f32_f16_e32 v86, v194, v194
	v_dot2c_f32_f16_e32 v86, v195, v195
	v_mfma_f32_16x16x32_f16 v[82:85], v[194:197], v[202:205], v[82:85]
	v_dot2c_f32_f16_e32 v86, v196, v196
	v_dot2c_f32_f16_e32 v86, v197, v197
	ds_read_b128 v[194:197], v142 offset:256
	ds_read_b128 v[198:201], v136 offset:256
	ds_read_b128 v[202:205], v136 offset:9984
	s_waitcnt lgkmcnt(9)
	v_mfma_f32_16x16x32_f16 v[78:81], v[206:209], v[210:213], v[78:81]
	v_dot2c_f32_f16_e32 v86, v206, v206
	v_dot2c_f32_f16_e32 v86, v207, v207
	v_mfma_f32_16x16x32_f16 v[82:85], v[206:209], v[214:217], v[82:85]
	v_dot2c_f32_f16_e32 v86, v208, v208
	v_dot2c_f32_f16_e32 v86, v209, v209
	ds_read_b128 v[206:209], v142 offset:320
	ds_read_b128 v[210:213], v136 offset:320
	ds_read_b128 v[214:217], v136 offset:10048
	s_waitcnt lgkmcnt(9)
	v_mfma_f32_16x16x32_f16 v[78:81], v[218:221], v[222:225], v[78:81]
	v_dot2c_f32_f16_e32 v86, v218, v218
	v_dot2c_f32_f16_e32 v86, v219, v219
	v_mfma_f32_16x16x32_f16 v[82:85], v[218:221], v[226:229], v[82:85]
	v_dot2c_f32_f16_e32 v86, v220, v220
	v_dot2c_f32_f16_e32 v86, v221, v221
	s_waitcnt lgkmcnt(6)
	v_mfma_f32_16x16x32_f16 v[78:81], v[230:233], v[234:237], v[78:81]
	v_dot2c_f32_f16_e32 v86, v230, v230
	v_dot2c_f32_f16_e32 v86, v231, v231
	v_mfma_f32_16x16x32_f16 v[82:85], v[230:233], v[238:241], v[82:85]
	v_dot2c_f32_f16_e32 v86, v232, v232
	v_dot2c_f32_f16_e32 v86, v233, v233
	s_waitcnt lgkmcnt(3)
	v_mfma_f32_16x16x32_f16 v[78:81], v[194:197], v[198:201], v[78:81]
	v_dot2c_f32_f16_e32 v86, v194, v194
	v_dot2c_f32_f16_e32 v86, v195, v195
	v_mfma_f32_16x16x32_f16 v[82:85], v[194:197], v[202:205], v[82:85]
	v_dot2c_f32_f16_e32 v86, v196, v196
	v_dot2c_f32_f16_e32 v86, v197, v197
	s_waitcnt lgkmcnt(0)
	v_mfma_f32_16x16x32_f16 v[78:81], v[206:209], v[210:213], v[78:81]
	v_dot2c_f32_f16_e32 v86, v206, v206
	v_dot2c_f32_f16_e32 v86, v207, v207
	v_mfma_f32_16x16x32_f16 v[82:85], v[206:209], v[214:217], v[82:85]
	v_dot2c_f32_f16_e32 v86, v208, v208
	v_dot2c_f32_f16_e32 v86, v209, v209
	ds_read_b128 v[222:225], v136 offset:384
	ds_read_b128 v[226:229], v136 offset:10112
	ds_read_b128 v[234:237], v136 offset:448
	ds_read_b128 v[238:241], v136 offset:10176
	ds_read_b128 v[198:201], v136 offset:512
	ds_read_b128 v[202:205], v136 offset:10240
	ds_read2st64_b64 v[88:91], v160 offset0:1 offset1:20
	s_waitcnt vmcnt(0)
	v_cvt_pk_f16_f32 v163, v188, v189
	v_cvt_pk_f16_f32 v162, v186, v187
	s_and_saveexec_b64 s[12:13], s[8:9]
	ds_write_b64 v150, v[162:163] offset:19456
	s_or_b64 exec, exec, s[12:13]
	ds_read_b128 v[218:221], v142 offset:384
	ds_read_b128 v[230:233], v142 offset:448
	ds_read_b128 v[194:197], v142 offset:512
	ds_read_b64 v[92:93], v159 offset:20032
	s_waitcnt lgkmcnt(3)
	v_mfma_f32_16x16x32_f16 v[78:81], v[218:221], v[222:225], v[78:81]
	v_dot2c_f32_f16_e32 v86, v218, v218
	v_dot2c_f32_f16_e32 v86, v219, v219
	v_mfma_f32_16x16x32_f16 v[82:85], v[218:221], v[226:229], v[82:85]
	v_dot2c_f32_f16_e32 v86, v220, v220
	v_dot2c_f32_f16_e32 v86, v221, v221
	s_waitcnt lgkmcnt(2)
	v_mfma_f32_16x16x32_f16 v[78:81], v[230:233], v[234:237], v[78:81]
	v_dot2c_f32_f16_e32 v86, v230, v230
	v_dot2c_f32_f16_e32 v86, v231, v231
	v_mfma_f32_16x16x32_f16 v[82:85], v[230:233], v[238:241], v[82:85]
	v_dot2c_f32_f16_e32 v86, v232, v232
	v_dot2c_f32_f16_e32 v86, v233, v233
	s_waitcnt lgkmcnt(1)
	v_mfma_f32_16x16x32_f16 v[78:81], v[194:197], v[198:201], v[78:81]
	v_dot2c_f32_f16_e32 v86, v194, v194
	v_dot2c_f32_f16_e32 v86, v195, v195
	v_mfma_f32_16x16x32_f16 v[82:85], v[194:197], v[202:205], v[82:85]
	v_dot2c_f32_f16_e32 v86, v196, v196
	v_dot2c_f32_f16_e32 v86, v197, v197
	s_waitcnt lgkmcnt(0)
	v_mfma_f32_16x16x16_f16 v[78:81], v[92:93], v[88:89], v[78:81]
	v_dot2c_f32_f16_e32 v86, v92, v92
	v_dot2c_f32_f16_e32 v86, v93, v93
	v_mfma_f32_16x16x16_f16 v[82:85], v[92:93], v[90:91], v[82:85]
	s_branch .Lnorm
